# speedup vs baseline: 1.0302x; 1.0302x over previous
.LBB1_2:
	s_or_saveexec_b64 s[2:3], s[2:3]
	v_mad_i32_i24 v170, v167, s4, v165
	s_xor_b64 exec, exec, s[2:3]
	s_cbranch_execz .LBB1_4
	s_setprio 1
	v_mad_u32_u24 v18, v167, 20, v170
	s_movk_i32 s4, 0x50
	v_mad_u64_u32 v[208:209], s[4:5], v18, s4, v[162:163]
	ds_read_b128 v[34:37], v171
	ds_read_b128 v[38:41], v171 offset:32
	ds_read_b128 v[42:45], v171 offset:80
	ds_read_b128 v[46:49], v171 offset:112
	ds_read_b128 v[172:175], v171 offset:160
	ds_read_b128 v[176:179], v171 offset:192
	ds_read_b128 v[180:183], v171 offset:1600
	ds_read_b128 v[184:187], v171 offset:1632
	ds_read_b128 v[188:191], v171 offset:1680
	s_waitcnt vmcnt(12) lgkmcnt(8)
	v_mfma_f32_32x32x16_f16 v[18:33], v[150:153], v[34:37], v[2:17]
	s_waitcnt lgkmcnt(7)
	v_mfma_f32_32x32x16_f16 v[18:33], v[146:149], v[38:41], v[18:33]
	ds_read_b128 v[34:37], v171 offset:1712
	s_waitcnt lgkmcnt(7)
	v_mfma_f32_32x32x16_f16 v[18:33], v[142:145], v[42:45], v[18:33]
	ds_read_b128 v[38:41], v171 offset:1760
	s_waitcnt lgkmcnt(7)
	v_mfma_f32_32x32x16_f16 v[18:33], v[138:141], v[46:49], v[18:33]
	ds_read_b128 v[42:45], v171 offset:1792
	s_waitcnt lgkmcnt(7)
	v_mfma_f32_32x32x16_f16 v[18:33], v[134:137], v[172:175], v[18:33]
	ds_read_b128 v[46:49], v171 offset:3200
	s_waitcnt lgkmcnt(7)
	v_mfma_f32_32x32x16_f16 v[18:33], v[130:133], v[176:179], v[18:33]
	ds_read_b128 v[172:175], v171 offset:3232
	s_waitcnt lgkmcnt(7)
	v_mfma_f32_32x32x16_f16 v[18:33], v[126:129], v[180:183], v[18:33]
	ds_read_b128 v[176:179], v171 offset:3280
	s_waitcnt lgkmcnt(7)
	v_mfma_f32_32x32x16_f16 v[18:33], v[122:125], v[184:187], v[18:33]
	ds_read_b128 v[180:183], v171 offset:3312
	s_waitcnt lgkmcnt(7)
	v_mfma_f32_32x32x16_f16 v[18:33], v[118:121], v[188:191], v[18:33]
	ds_read_b128 v[184:187], v171 offset:3360
	s_waitcnt lgkmcnt(7)
	v_mfma_f32_32x32x16_f16 v[18:33], v[114:117], v[34:37], v[18:33]
	ds_read_b128 v[188:191], v171 offset:3392
	s_waitcnt lgkmcnt(7)
	v_mfma_f32_32x32x16_f16 v[18:33], v[110:113], v[38:41], v[18:33]
	ds_read_b128 v[192:195], v208
	s_waitcnt lgkmcnt(7)
	v_mfma_f32_32x32x16_f16 v[18:33], v[106:109], v[42:45], v[18:33]
	ds_read_b128 v[196:199], v208 offset:32
	s_waitcnt lgkmcnt(7)
	v_mfma_f32_32x32x16_f16 v[18:33], v[102:105], v[46:49], v[18:33]
	ds_read_b128 v[200:203], v208 offset:80
	s_waitcnt lgkmcnt(7)
	v_mfma_f32_32x32x16_f16 v[18:33], v[98:101], v[172:175], v[18:33]
	ds_read_b128 v[204:207], v208 offset:112
	s_waitcnt lgkmcnt(7)
	v_mfma_f32_32x32x16_f16 v[18:33], v[94:97], v[176:179], v[18:33]
	ds_read_b128 v[172:175], v208 offset:160
	s_waitcnt lgkmcnt(7)
	v_mfma_f32_32x32x16_f16 v[18:33], v[90:93], v[180:183], v[18:33]
	ds_read_b128 v[176:179], v208 offset:192
	s_waitcnt lgkmcnt(7)
	v_mfma_f32_32x32x16_f16 v[18:33], v[86:89], v[184:187], v[18:33]
	ds_read_b128 v[180:183], v208 offset:1600
	s_waitcnt lgkmcnt(7)
	v_mfma_f32_32x32x16_f16 v[18:33], v[82:85], v[188:191], v[18:33]
	ds_read_b128 v[184:187], v208 offset:1632
	s_waitcnt lgkmcnt(7)
	v_mfma_f32_32x32x16_f16 v[34:49], v[150:153], v[192:195], v[2:17]
	ds_read_b128 v[188:191], v208 offset:1680
	s_waitcnt lgkmcnt(7)
	v_mfma_f32_32x32x16_f16 v[34:49], v[146:149], v[196:199], v[34:49]
	ds_read_b128 v[192:195], v208 offset:1712
	s_waitcnt lgkmcnt(7)
	v_mfma_f32_32x32x16_f16 v[34:49], v[142:145], v[200:203], v[34:49]
	ds_read_b128 v[196:199], v208 offset:1760
	s_waitcnt lgkmcnt(7)
	v_mfma_f32_32x32x16_f16 v[34:49], v[138:141], v[204:207], v[34:49]
	ds_read_b128 v[200:203], v208 offset:1792
	s_waitcnt lgkmcnt(7)
	v_mfma_f32_32x32x16_f16 v[34:49], v[134:137], v[172:175], v[34:49]
	ds_read_b128 v[204:207], v208 offset:3200
	s_waitcnt lgkmcnt(7)
	v_mfma_f32_32x32x16_f16 v[34:49], v[130:133], v[176:179], v[34:49]
	ds_read_b128 v[172:175], v208 offset:3232
	s_waitcnt lgkmcnt(7)
	v_mfma_f32_32x32x16_f16 v[34:49], v[126:129], v[180:183], v[34:49]
	ds_read_b128 v[176:179], v208 offset:3280
	s_waitcnt lgkmcnt(7)
	v_mfma_f32_32x32x16_f16 v[34:49], v[122:125], v[184:187], v[34:49]
	ds_read_b128 v[180:183], v208 offset:3312
	s_waitcnt lgkmcnt(7)
	v_mfma_f32_32x32x16_f16 v[34:49], v[118:121], v[188:191], v[34:49]
	ds_read_b128 v[184:187], v208 offset:3360
	s_waitcnt lgkmcnt(7)
	v_mfma_f32_32x32x16_f16 v[34:49], v[114:117], v[192:195], v[34:49]
	ds_read_b128 v[188:191], v208 offset:3392
	s_waitcnt lgkmcnt(7)
	v_mfma_f32_32x32x16_f16 v[34:49], v[110:113], v[196:199], v[34:49]
	s_waitcnt lgkmcnt(6)
	v_mfma_f32_32x32x16_f16 v[34:49], v[106:109], v[200:203], v[34:49]
	s_waitcnt lgkmcnt(5)
	v_mfma_f32_32x32x16_f16 v[34:49], v[102:105], v[204:207], v[34:49]
	s_waitcnt lgkmcnt(4)
	v_mfma_f32_32x32x16_f16 v[34:49], v[98:101], v[172:175], v[34:49]
	s_waitcnt lgkmcnt(3)
	v_mfma_f32_32x32x16_f16 v[34:49], v[94:97], v[176:179], v[34:49]
	s_waitcnt lgkmcnt(2)
	v_mfma_f32_32x32x16_f16 v[34:49], v[90:93], v[180:183], v[34:49]
	s_waitcnt lgkmcnt(1)
	v_mfma_f32_32x32x16_f16 v[34:49], v[86:89], v[184:187], v[34:49]
	s_waitcnt lgkmcnt(0)
	v_mfma_f32_32x32x16_f16 v[34:49], v[82:85], v[188:191], v[34:49]
.LBB1_4:
	s_or_b64 exec, exec, s[2:3]
	s_setprio 0
	s_movk_i32 s2, 0x144
	s_add_i32 s12, s12, -1
	s_add_i32 s13, s13, -1
	v_and_b32_e32 v171, 32, v0
	v_cmp_gt_u32_e64 s[2:3], s2, v166
	s_and_saveexec_b64 s[4:5], s[2:3]
	s_cbranch_execz .LBB1_6
	v_add_u32_e32 v168, s12, v168
	v_add_u32_e32 v169, s13, v169
	v_max_u32_e32 v168, v168, v169
	s_movk_i32 s2, 0x50
	v_cvt_pk_f16_f32 v18, v18, v19
	v_cvt_pk_f16_f32 v19, v26, v27
	v_mad_u32_u24 v169, v166, s2, v171
	v_cmp_gt_u32_e64 s[2:3], 64, v168
	v_pk_max_f16 v19, v19, 0
	v_pk_max_f16 v18, v18, 0
	v_cndmask_b32_e64 v26, 0, v19, s[2:3]
	v_cvt_pk_f16_f32 v19, v20, v21
	v_cvt_pk_f16_f32 v20, v28, v29
	v_cvt_pk_f16_f32 v21, v30, v31
	v_pk_max_f16 v20, v20, 0
	v_pk_max_f16 v21, v21, 0
	v_cndmask_b32_e64 v27, 0, v20, s[2:3]
	v_cvt_pk_f16_f32 v20, v22, v23
	v_cndmask_b32_e64 v28, 0, v21, s[2:3]
	v_cvt_pk_f16_f32 v21, v24, v25
	v_pk_max_f16 v19, v19, 0
	v_pk_max_f16 v20, v20, 0
	v_pk_max_f16 v21, v21, 0
	v_cvt_pk_f16_f32 v22, v32, v33
	v_cndmask_b32_e64 v18, 0, v18, s[2:3]
	v_cndmask_b32_e64 v19, 0, v19, s[2:3]
	v_cndmask_b32_e64 v20, 0, v20, s[2:3]
	v_cndmask_b32_e64 v21, 0, v21, s[2:3]
	v_pk_max_f16 v22, v22, 0
	s_nop 0
	v_cndmask_b32_e64 v29, 0, v22, s[2:3]
	ds_write_b128 v169, v[18:21] offset:32000
	ds_write_b128 v169, v[26:29] offset:32016
